# RG-LRU conv step: 6 iterations unrolled, LDS constant/tap reads batched (3x14) instead of three waits per element
# baseline (speedup 1.0000x reference)
.LBB0_546:
	s_waitcnt lgkmcnt(0)
	s_barrier
	s_and_saveexec_b64 s[16:17], s[12:13]
	s_cbranch_execz .LBB0_549
	v_mul_hi_i32 v132, v28, s83
	v_lshrrev_b32_e32 v134, 31, v132
	v_ashrrev_i32_e32 v132, 3, v132
	v_add_u32_e32 v132, v132, v134
	v_mov_b32_e32 v133, v51
	v_mad_i32_i24 v134, v132, s86, v133
	v_add_u32_e32 v134, 0x15b80, v134
	v_add_u32_e32 v144, 512, v28
	v_mul_hi_i32 v144, v144, s83
	v_lshrrev_b32_e32 v146, 31, v144
	v_ashrrev_i32_e32 v144, 3, v144
	v_add_u32_e32 v144, v144, v146
	v_add_u32_e32 v145, 2048, v51
	v_mad_i32_i24 v146, v144, s86, v145
	v_add_u32_e32 v146, 0x15b80, v146
	v_add_u32_e32 v162, 1024, v28
	v_mul_hi_i32 v162, v162, s83
	v_lshrrev_b32_e32 v164, 31, v162
	v_ashrrev_i32_e32 v162, 3, v162
	v_add_u32_e32 v162, v162, v164
	v_add_u32_e32 v163, 4096, v51
	v_mad_i32_i24 v164, v162, s86, v163
	v_add_u32_e32 v164, 0x15b80, v164
	v_add_u32_e32 v174, 1536, v28
	v_mul_hi_i32 v174, v174, s83
	v_lshrrev_b32_e32 v176, 31, v174
	v_ashrrev_i32_e32 v174, 3, v174
	v_add_u32_e32 v174, v174, v176
	v_add_u32_e32 v175, 6144, v51
	v_mad_i32_i24 v176, v174, s86, v175
	v_add_u32_e32 v176, 0x15b80, v176
	v_add_u32_e32 v186, 2048, v28
	v_mul_hi_i32 v186, v186, s83
	v_lshrrev_b32_e32 v188, 31, v186
	v_ashrrev_i32_e32 v186, 3, v186
	v_add_u32_e32 v186, v186, v188
	v_add_u32_e32 v187, 8192, v51
	v_mad_i32_i24 v188, v186, s86, v187
	v_add_u32_e32 v188, 0x15b80, v188
	v_add_u32_e32 v198, 2560, v28
	v_mul_hi_i32 v198, v198, s83
	v_lshrrev_b32_e32 v200, 31, v198
	v_ashrrev_i32_e32 v198, 3, v198
	v_add_u32_e32 v198, v198, v200
	v_add_u32_e32 v199, 10240, v51
	v_mad_i32_i24 v200, v198, s86, v199
	v_add_u32_e32 v200, 0x15b80, v200
	ds_read_b32 v135, v134
	ds_read_b32 v136, v134 offset:192
	ds_read2_b32 v[140:141], v133 offset1:48
	ds_read_b32 v137, v134 offset:384
	ds_read_b32 v138, v134 offset:576
	ds_read2_b32 v[142:143], v133 offset0:96 offset1:144
	ds_read_b32 v139, v134 offset:768
	ds_read_b32 v147, v146
	ds_read_b32 v148, v146 offset:192
	ds_read2_b32 v[152:153], v145 offset1:48
	ds_read_b32 v149, v146 offset:384
	ds_read_b32 v150, v146 offset:576
	ds_read2_b32 v[154:155], v145 offset0:96 offset1:144
	ds_read_b32 v151, v146 offset:768
	s_waitcnt lgkmcnt(0)
	ds_read_b32 v165, v164
	ds_read_b32 v166, v164 offset:192
	ds_read2_b32 v[170:171], v163 offset1:48
	ds_read_b32 v167, v164 offset:384
	ds_read_b32 v168, v164 offset:576
	ds_read2_b32 v[172:173], v163 offset0:96 offset1:144
	ds_read_b32 v169, v164 offset:768
	ds_read_b32 v177, v176
	ds_read_b32 v178, v176 offset:192
	ds_read2_b32 v[182:183], v175 offset1:48
	ds_read_b32 v179, v176 offset:384
	ds_read_b32 v180, v176 offset:576
	ds_read2_b32 v[184:185], v175 offset0:96 offset1:144
	ds_read_b32 v181, v176 offset:768
	v_fmac_f32_e32 v135, v136, v140
	v_fmac_f32_e32 v147, v148, v152
	v_fmac_f32_e32 v135, v137, v141
	v_fmac_f32_e32 v147, v149, v153
	v_fmac_f32_e32 v135, v138, v142
	v_fmac_f32_e32 v147, v150, v154
	v_fmac_f32_e32 v135, v139, v143
	v_fmac_f32_e32 v147, v151, v155
	ds_write_b32 v133, v135 offset:12864
	v_bfe_u32 v136, v135, 16, 1
	v_lshl_add_u32 v137, v132, 4, v93
	v_add3_u32 v136, v135, v136, s87
	ds_write_b16_d16_hi v137, v136
	ds_write_b32 v145, v147 offset:12864
	v_bfe_u32 v148, v147, 16, 1
	v_lshl_add_u32 v149, v144, 4, v93
	v_add3_u32 v148, v147, v148, s87
	ds_write_b16_d16_hi v149, v148 offset:1024
	s_waitcnt lgkmcnt(0)
	ds_read_b32 v189, v188
	ds_read_b32 v190, v188 offset:192
	ds_read2_b32 v[194:195], v187 offset1:48
	ds_read_b32 v191, v188 offset:384
	ds_read_b32 v192, v188 offset:576
	ds_read2_b32 v[196:197], v187 offset0:96 offset1:144
	ds_read_b32 v193, v188 offset:768
	ds_read_b32 v201, v200
	ds_read_b32 v202, v200 offset:192
	ds_read2_b32 v[206:207], v199 offset1:48
	ds_read_b32 v203, v200 offset:384
	ds_read_b32 v204, v200 offset:576
	ds_read2_b32 v[208:209], v199 offset0:96 offset1:144
	ds_read_b32 v205, v200 offset:768
	v_fmac_f32_e32 v165, v166, v170
	v_fmac_f32_e32 v177, v178, v182
	v_fmac_f32_e32 v165, v167, v171
	v_fmac_f32_e32 v177, v179, v183
	v_fmac_f32_e32 v165, v168, v172
	v_fmac_f32_e32 v177, v180, v184
	v_fmac_f32_e32 v165, v169, v173
	v_fmac_f32_e32 v177, v181, v185
	ds_write_b32 v163, v165 offset:12864
	v_bfe_u32 v166, v165, 16, 1
	v_lshl_add_u32 v167, v162, 4, v93
	v_add3_u32 v166, v165, v166, s87
	ds_write_b16_d16_hi v167, v166 offset:2048
	ds_write_b32 v175, v177 offset:12864
	v_bfe_u32 v178, v177, 16, 1
	v_lshl_add_u32 v179, v174, 4, v93
	v_add3_u32 v178, v177, v178, s87
	ds_write_b16_d16_hi v179, v178 offset:3072
	s_waitcnt lgkmcnt(0)
	v_fmac_f32_e32 v189, v190, v194
	v_fmac_f32_e32 v201, v202, v206
	v_fmac_f32_e32 v189, v191, v195
	v_fmac_f32_e32 v201, v203, v207
	v_fmac_f32_e32 v189, v192, v196
	v_fmac_f32_e32 v201, v204, v208
	v_fmac_f32_e32 v189, v193, v197
	v_fmac_f32_e32 v201, v205, v209
	ds_write_b32 v187, v189 offset:12864
	v_bfe_u32 v190, v189, 16, 1
	v_lshl_add_u32 v191, v186, 4, v93
	v_add3_u32 v190, v189, v190, s87
	ds_write_b16_d16_hi v191, v190 offset:4096
	ds_write_b32 v199, v201 offset:12864
	v_bfe_u32 v202, v201, 16, 1
	v_lshl_add_u32 v203, v198, 4, v93
	v_add3_u32 v202, v201, v202, s87
	ds_write_b16_d16_hi v203, v202 offset:5120
